# top-k phase carries 4 MoE-weight conversion items per wave (loads issued at phase start, transposes after selection); GOUT idle slot converts 8192 items fewer
# baseline (speedup 1.0000x reference)
; #define LAS __attribute__((address_space(3)))
; #define PHASE_FRAME(F0) Frame F = F0; { int t_ = threadIdx.x; asm volatile("" : "+v"(t_)); F.tid = t_; F.lane = t_ & 63; F.wave = __builtin_amdgcn_readfirstlane(t_ >> 6); }
; __device__ __forceinline__ void moe_convert_slice(const Frame& F0, int L, int first, int n, int rank, int n_idle) {
;     PHASE_FRAME(F0);
;     const int per = (n + n_idle - 1) / n_idle, lo = first + rank * per, hi = (lo + per < first + n) ? lo + per : first + n;
;     moe_convert_run(F, L, lo + F.wave, hi, 8, (LAS float*)(F.lds + F.wave * 16384));
; }
; __global__ void __launch_bounds__(512, 2) mk_fwd(Args args) {
;     ...
;             if (with_ctx && blockIdx.x >= 64) moe_convert_slice(F, L + 1, 0, CV_C1(L + 1), (int)blockIdx.x - 64, 192);
.LBB0_1089:
	v_readlane_b32 s0, v254, 2
	v_readlane_b32 s2, v255, 14
	v_readlane_b32 s1, v254, 3
	v_readlane_b32 s3, v255, 15
	s_and_b64 s[0:1], s[0:1], s[2:3]
	s_andn2_b64 vcc, exec, s[0:1]
	s_cbranch_vccnz .LBB0_1144
	v_readlane_b32 s2, v255, 17
	s_add_i32 s7, s2, 1
	s_cmp_eq_u32 s7, 2
	s_movk_i32 s0, 0x1c00
	s_cselect_b32 s0, 0x1000, s0
	s_cmp_lg_u32 s2, 0
	s_waitcnt vmcnt(0) lgkmcnt(0)
	v_mov_b32_e32 v2, v0
	s_cselect_b32 s0, s0, 0x1600
	v_readlane_b32 s2, v254, 4
	v_readfirstlane_b32 s1, v2
	s_ashr_i32 s8, s1, 6
	s_or_b32 s1, s0, 0x80
	s_mulk_i32 s1, 0x2aab
	s_lshr_b32 s1, s1, 21
	s_mul_i32 s2, s2, s1
	s_add_i32 s1, s2, s1
	s_min_i32 s12, s1, s0
	s_add_i32 s4, s8, s2
	s_cmp_ge_i32 s4, s12
	v_readlane_b32 s3, v255, 18
	s_cbranch_scc1 .LBB0_1144
	s_ashr_i32 s0, s4, 31
	s_lshr_b32 s0, s0, 23
	s_add_i32 s0, s4, s0
	s_ashr_i32 s6, s0, 9
	s_mul_hi_i32 s0, s6, 0x55555556
	s_lshr_b32 s1, s0, 31
	s_add_i32 s0, s0, s1
	s_mul_i32 s0, s0, 3
	s_sub_i32 s5, s6, s0
	s_cmp_eq_u32 s5, 0
	s_cselect_b64 s[2:3], -1, 0
	s_cmp_lg_u32 s5, 0
	s_mov_b64 s[0:1], -1
	s_cbranch_scc0 .LBB0_1097
	s_cmp_lg_u32 s5, 1
	s_cbranch_scc0 .LBB0_1094
	v_readlane_b32 s0, v255, 5
	s_nop 1
	v_mov_b32_e32 v1, s0
	ds_read_b64 v[4:5], v1
	s_mov_b64 s[0:1], 0
	s_waitcnt lgkmcnt(0)
	v_readfirstlane_b32 s9, v4
	v_readfirstlane_b32 s10, v5

; #define LAS __attribute__((address_space(3)))
; __device__ __forceinline__ TItem moe_item(Frame& F, int L, int r) {
;     constexpr int I_SQ = 16 * (1024 / 32);
;     const int mi = r / I_SQ, item = r % I_SQ, e = mi / 3, which = mi % 3;
;     const float* W = (which == 0 ? inp(F, I_WG) : which == 1 ? inp(F, I_WU) : inp(F, I_WD)) + (size_t)(L * 16 + e) * 1024 * 1024;
;     bf16_t* WT = (bf16_t*)(which < 2 ? F.ws + WS_WUP + (size_t)(L * 16 + e) * 2048 * 1024 : F.ws + WS_WDN + (size_t)(L * 16 + e) * 1024 * 1024);
;     return TItem{W, WT, 1024, which == 0 ? RM_UPG : which == 1 ? RM_UPU : RM_P8, item, true};
; }
; __device__ __forceinline__ void moe_convert_run(Frame& F, int L, int first, int end, int stride, LAS float* scr) {
;     if (first >= end) return;
;     f32x4 nv[8]; TItem nT = moe_item(F, L, first); titem_load(nT, F.lane, nv);
.LBB0_1270:
	s_andn2_b64 vcc, exec, s[0:1]
	s_cbranch_vccnz .LBB0_1388
	v_readlane_b32 s0, v254, 9
	v_mov_b32_e32 v1, v0
	v_readlane_b32 s1, v254, 10
	s_mov_b32 s4, 0
	v_writelane_b32 v255, s4, 56
	s_andn2_b64 vcc, exec, s[0:1]
	v_readfirstlane_b32 s0, v1
	s_cbranch_vccnz .LBB0_1334
	v_readlane_b32 s4, v255, 17
	s_cmp_eq_u32 s4, 3
	s_cbranch_scc1 .Ltkcv_a_done
	s_add_i32 s5, s4, 1
	s_lshl_b32 s17, s5, 4
	s_cmp_eq_u32 s4, 0
	s_movk_i32 s5, 0x1c00
	s_cselect_b32 s5, 0x1600, s5
	s_cmp_eq_u32 s4, 1
	s_cselect_b32 s5, 0x1000, s5
	v_readfirstlane_b32 s6, v0
	s_nop 3
	s_lshr_b32 s6, s6, 6
	s_lshl_b32 s7, s84, 5
	s_add_i32 s6, s6, s7
	s_mul_i32 s6, s6, 1
	s_add_i32 s22, s5, s6
	v_bfe_u32 v54, v0, 3, 3
	v_and_b32_e32 v56, 7, v0
	v_lshlrev_b32_e32 v56, 4, v56
	v_mov_b32_e32 v57, 0
	s_ashr_i32 s4, s22, 31
	s_lshr_b32 s4, s4, 23
	s_add_i32 s4, s22, s4
	s_ashr_i32 s8, s4, 9
	s_mul_hi_i32 s4, s8, 0x55555556
	s_lshr_b32 s5, s4, 31
	s_add_i32 s4, s4, s5
	s_mul_i32 s4, s4, 3
	s_sub_i32 s9, s8, s4
	s_cmp_eq_u32 s9, 0
	s_cselect_b64 s[6:7], -1, 0
	s_cmp_lg_u32 s9, 0
	s_mov_b64 s[4:5], -1
	s_cbranch_scc0 .Ltkcv_a0_1525
	s_cmp_lg_u32 s9, 1
	s_cbranch_scc0 .Ltkcv_a0_1522
	v_readlane_b32 s4, v255, 5
	s_nop 1
	v_mov_b32_e32 v76, s4
	ds_read_b64 v[76:77], v76
	s_mov_b64 s[4:5], 0
	s_waitcnt lgkmcnt(0)
	v_readfirstlane_b32 s11, v76
	v_readfirstlane_b32 s18, v77
.Ltkcv_a0_1522:
	s_andn2_b64 vcc, exec, s[4:5]
	s_cbranch_vccnz .Ltkcv_a0_1524
	v_readlane_b32 s4, v255, 6
	s_nop 1
	v_mov_b32_e32 v76, s4
	ds_read_b64 v[76:77], v76
	s_waitcnt lgkmcnt(0)
	v_readfirstlane_b32 s11, v76
	v_readfirstlane_b32 s18, v77

; #define GAS __attribute__((address_space(1)))
; __device__ __forceinline__ void titem_load(const TItem& T, int lane, f32x4 (&v)[8]) {
;     const int nblk = T.N / 32, kb = T.item / nblk, nb = T.item % nblk, k0 = 64 * kb, n0 = 32 * nb;
; #pragma unroll
;     for (int i = 0; i < 8; ++i) v[i] = *(const GAS f32x4*)(T.W + (size_t)(k0 + 8 * i + (lane >> 3)) * T.N + n0 + 4 * (lane & 7));
; }
; __device__ __forceinline__ TItem moe_item(Frame& F, int L, int r) {
;     constexpr int I_SQ = 16 * (1024 / 32);
;     const int mi = r / I_SQ, item = r % I_SQ, e = mi / 3, which = mi % 3;
;     const float* W = (which == 0 ? inp(F, I_WG) : which == 1 ? inp(F, I_WU) : inp(F, I_WD)) + (size_t)(L * 16 + e) * 1024 * 1024;
;     bf16_t* WT = (bf16_t*)(which < 2 ? F.ws + WS_WUP + (size_t)(L * 16 + e) * 2048 * 1024 : F.ws + WS_WDN + (size_t)(L * 16 + e) * 1024 * 1024);
;     return TItem{W, WT, 1024, which == 0 ? RM_UPG : which == 1 ? RM_UPU : RM_P8, item, true};
; }
.Ltkcv_a0_1525:
	s_andn2_b64 vcc, exec, s[4:5]
	s_cbranch_vccnz .Ltkcv_a0_1527
	v_readlane_b32 s4, v255, 7
	s_nop 1
	v_mov_b32_e32 v76, s4
	ds_read_b64 v[76:77], v76
	s_waitcnt lgkmcnt(0)
	v_readfirstlane_b32 s11, v76
	v_readfirstlane_b32 s18, v77
.Ltkcv_a0_1527:
	s_mul_hi_i32 s4, s22, 0x2aaaaaab
	s_lshr_b32 s5, s4, 31
	s_ashr_i32 s4, s4, 8
	s_add_i32 s4, s4, s5
	s_add_i32 s28, s4, s17
	s_ashr_i32 s29, s28, 31
	s_lshl_b64 s[4:5], s[28:29], 20
	s_lshl_b64 s[30:31], s[28:29], 21
	v_readlane_b32 s19, v253, 45
	s_add_u32 s19, s19, s30
	v_readlane_b32 s25, v253, 46
	s_addc_u32 s25, s25, s31
	v_readlane_b32 s30, v253, 43
	s_add_u32 s4, s30, s4
	v_readlane_b32 s30, v253, 44
	s_addc_u32 s5, s30, s5
	s_cmp_lt_i32 s9, 2
	s_cselect_b32 s5, s25, s5
	s_cselect_b32 s4, s19, s4
	s_cmp_eq_u32 s9, 1
	s_cselect_b32 s9, 5, 2
	s_and_b64 s[6:7], s[6:7], exec
	s_cselect_b32 s25, 4, s9
	s_lshl_b64 s[6:7], s[28:29], 22
	s_add_u32 s6, s11, s6
	s_addc_u32 s7, s18, s7
	s_lshl_b32 s8, s8, 9
	s_sub_i32 s28, s22, s8
	s_sext_i32_i16 s8, s28
	s_bfe_u32 s8, s8, 0x5001a
	s_add_i32 s8, s28, s8
	s_sext_i32_i16 s9, s8
	s_lshl_b32 s9, s9, 1
	s_andn2_b32 s9, s9, 63
	s_and_b32 s8, s8, 0xffe0
	v_or_b32_e32 v100, s9, v54
	s_sub_i32 s8, s28, s8
	v_ashrrev_i32_e32 v101, 31, v100
	s_sext_i32_i16 s8, s8
	v_lshlrev_b64 v[76:77], 12, v[100:101]
	v_or_b32_e32 v78, 8, v100
	v_or_b32_e32 v84, 16, v100
	v_or_b32_e32 v86, 24, v100
	v_or_b32_e32 v92, 32, v100
	v_or_b32_e32 v94, 40, v100
	v_or_b32_e32 v102, 48, v100
	v_or_b32_e32 v100, 56, v100
	s_lshl_b32 s8, s8, 5
	v_ashrrev_i32_e32 v79, 31, v78
	v_ashrrev_i32_e32 v85, 31, v84
	v_ashrrev_i32_e32 v87, 31, v86
	v_ashrrev_i32_e32 v93, 31, v92
	v_ashrrev_i32_e32 v95, 31, v94
	v_ashrrev_i32_e32 v103, 31, v102
	v_ashrrev_i32_e32 v101, 31, v100
	s_ashr_i32 s9, s8, 31
	v_lshlrev_b64 v[78:79], 12, v[78:79]
	v_lshlrev_b64 v[84:85], 12, v[84:85]
	v_lshlrev_b64 v[86:87], 12, v[86:87]
	v_lshlrev_b64 v[92:93], 12, v[92:93]
	v_lshlrev_b64 v[94:95], 12, v[94:95]
	v_lshlrev_b64 v[102:103], 12, v[102:103]
	v_lshlrev_b64 v[100:101], 12, v[100:101]
	v_lshl_add_u64 v[76:77], s[6:7], 0, v[76:77]
	s_lshl_b64 s[8:9], s[8:9], 2
	v_lshl_add_u64 v[78:79], s[6:7], 0, v[78:79]
	v_lshl_add_u64 v[84:85], s[6:7], 0, v[84:85]
	v_lshl_add_u64 v[86:87], s[6:7], 0, v[86:87]
	v_lshl_add_u64 v[92:93], s[6:7], 0, v[92:93]
	v_lshl_add_u64 v[94:95], s[6:7], 0, v[94:95]
	v_lshl_add_u64 v[102:103], s[6:7], 0, v[102:103]
	v_lshl_add_u64 v[100:101], s[6:7], 0, v[100:101]
	v_lshl_add_u64 v[76:77], v[76:77], 0, s[8:9]
	v_lshl_add_u64 v[78:79], v[78:79], 0, s[8:9]
	v_lshl_add_u64 v[84:85], v[84:85], 0, s[8:9]
	v_lshl_add_u64 v[86:87], v[86:87], 0, s[8:9]
	v_lshl_add_u64 v[92:93], v[92:93], 0, s[8:9]
	v_lshl_add_u64 v[94:95], v[94:95], 0, s[8:9]
	v_lshl_add_u64 v[102:103], v[102:103], 0, s[8:9]
	v_lshl_add_u64 v[100:101], v[100:101], 0, s[8:9]
	v_lshl_add_u64 v[76:77], v[76:77], 0, v[56:57]
	v_lshl_add_u64 v[80:81], v[78:79], 0, v[56:57]
	v_lshl_add_u64 v[84:85], v[84:85], 0, v[56:57]
	v_lshl_add_u64 v[88:89], v[86:87], 0, v[56:57]
	v_lshl_add_u64 v[92:93], v[92:93], 0, v[56:57]
	v_lshl_add_u64 v[96:97], v[94:95], 0, v[56:57]
	v_lshl_add_u64 v[102:103], v[102:103], 0, v[56:57]
	v_lshl_add_u64 v[104:105], v[100:101], 0, v[56:57]
	global_load_dwordx4 v[76:79], v[76:77], off nt
	s_nop 0
	global_load_dwordx4 v[80:83], v[80:81], off nt
	s_nop 0
	global_load_dwordx4 v[84:87], v[84:85], off nt
	s_nop 0
	global_load_dwordx4 v[88:91], v[88:89], off nt
	s_nop 0
	global_load_dwordx4 v[92:95], v[92:93], off nt
	s_nop 0
	global_load_dwordx4 v[96:99], v[96:97], off nt
	s_nop 0
	global_load_dwordx4 v[100:103], v[102:103], off nt
	s_nop 0
	global_load_dwordx4 v[104:107], v[104:105], off nt
	v_writelane_b32 v255, s28, 40
	v_writelane_b32 v255, s25, 41
	v_writelane_b32 v255, s4, 42
	v_writelane_b32 v255, s5, 43
	s_add_i32 s22, s22, 8
	s_ashr_i32 s4, s22, 31
	s_lshr_b32 s4, s4, 23
	s_add_i32 s4, s22, s4
	s_ashr_i32 s8, s4, 9
	s_mul_hi_i32 s4, s8, 0x55555556
	s_lshr_b32 s5, s4, 31
	s_add_i32 s4, s4, s5
	s_mul_i32 s4, s4, 3
	s_sub_i32 s9, s8, s4
	s_cmp_eq_u32 s9, 0
	s_cselect_b64 s[6:7], -1, 0
	s_cmp_lg_u32 s9, 0
	s_mov_b64 s[4:5], -1
	s_cbranch_scc0 .Ltkcv_a1_1525
	s_cmp_lg_u32 s9, 1
	s_cbranch_scc0 .Ltkcv_a1_1522
	v_readlane_b32 s4, v255, 5
	s_nop 1
	v_mov_b32_e32 v108, s4
	ds_read_b64 v[108:109], v108
	s_mov_b64 s[4:5], 0
	s_waitcnt lgkmcnt(0)
	v_readfirstlane_b32 s11, v108
	v_readfirstlane_b32 s18, v109
.Ltkcv_a1_1522:
	s_andn2_b64 vcc, exec, s[4:5]
	s_cbranch_vccnz .Ltkcv_a1_1524
	v_readlane_b32 s4, v255, 6
	s_nop 1
	v_mov_b32_e32 v108, s4
	ds_read_b64 v[108:109], v108
	s_waitcnt lgkmcnt(0)
	v_readfirstlane_b32 s11, v108
	v_readfirstlane_b32 s18, v109

; #define GAS __attribute__((address_space(1)))
; __device__ __forceinline__ void titem_load(const TItem& T, int lane, f32x4 (&v)[8]) {
;     const int nblk = T.N / 32, kb = T.item / nblk, nb = T.item % nblk, k0 = 64 * kb, n0 = 32 * nb;
; #pragma unroll
;     for (int i = 0; i < 8; ++i) v[i] = *(const GAS f32x4*)(T.W + (size_t)(k0 + 8 * i + (lane >> 3)) * T.N + n0 + 4 * (lane & 7));
; }
; __device__ __forceinline__ TItem moe_item(Frame& F, int L, int r) {
;     constexpr int I_SQ = 16 * (1024 / 32);
;     const int mi = r / I_SQ, item = r % I_SQ, e = mi / 3, which = mi % 3;
;     const float* W = (which == 0 ? inp(F, I_WG) : which == 1 ? inp(F, I_WU) : inp(F, I_WD)) + (size_t)(L * 16 + e) * 1024 * 1024;
;     bf16_t* WT = (bf16_t*)(which < 2 ? F.ws + WS_WUP + (size_t)(L * 16 + e) * 2048 * 1024 : F.ws + WS_WDN + (size_t)(L * 16 + e) * 1024 * 1024);
;     return TItem{W, WT, 1024, which == 0 ? RM_UPG : which == 1 ? RM_UPU : RM_P8, item, true};
; }
.Ltkcv_a1_1525:
	s_andn2_b64 vcc, exec, s[4:5]
	s_cbranch_vccnz .Ltkcv_a1_1527
	v_readlane_b32 s4, v255, 7
	s_nop 1
	v_mov_b32_e32 v108, s4
	ds_read_b64 v[108:109], v108
	s_waitcnt lgkmcnt(0)
	v_readfirstlane_b32 s11, v108
	v_readfirstlane_b32 s18, v109
.Ltkcv_a1_1527:
	s_mul_hi_i32 s4, s22, 0x2aaaaaab
	s_lshr_b32 s5, s4, 31
	s_ashr_i32 s4, s4, 8
	s_add_i32 s4, s4, s5
	s_add_i32 s28, s4, s17
	s_ashr_i32 s29, s28, 31
	s_lshl_b64 s[4:5], s[28:29], 20
	s_lshl_b64 s[30:31], s[28:29], 21
	v_readlane_b32 s19, v253, 45
	s_add_u32 s19, s19, s30
	v_readlane_b32 s25, v253, 46
	s_addc_u32 s25, s25, s31
	v_readlane_b32 s30, v253, 43
	s_add_u32 s4, s30, s4
	v_readlane_b32 s30, v253, 44
	s_addc_u32 s5, s30, s5
	s_cmp_lt_i32 s9, 2
	s_cselect_b32 s5, s25, s5
	s_cselect_b32 s4, s19, s4
	s_cmp_eq_u32 s9, 1
	s_cselect_b32 s9, 5, 2
	s_and_b64 s[6:7], s[6:7], exec
	s_cselect_b32 s25, 4, s9
	s_lshl_b64 s[6:7], s[28:29], 22
	s_add_u32 s6, s11, s6
	s_addc_u32 s7, s18, s7
	s_lshl_b32 s8, s8, 9
	s_sub_i32 s28, s22, s8
	s_sext_i32_i16 s8, s28
	s_bfe_u32 s8, s8, 0x5001a
	s_add_i32 s8, s28, s8
	s_sext_i32_i16 s9, s8
	s_lshl_b32 s9, s9, 1
	s_andn2_b32 s9, s9, 63
	s_and_b32 s8, s8, 0xffe0
	v_or_b32_e32 v132, s9, v54
	s_sub_i32 s8, s28, s8
	v_ashrrev_i32_e32 v133, 31, v132
	s_sext_i32_i16 s8, s8
	v_lshlrev_b64 v[108:109], 12, v[132:133]
	v_or_b32_e32 v110, 8, v132
	v_or_b32_e32 v116, 16, v132
	v_or_b32_e32 v118, 24, v132
	v_or_b32_e32 v124, 32, v132
	v_or_b32_e32 v126, 40, v132
	v_or_b32_e32 v134, 48, v132
	v_or_b32_e32 v132, 56, v132
	s_lshl_b32 s8, s8, 5
	v_ashrrev_i32_e32 v111, 31, v110
	v_ashrrev_i32_e32 v117, 31, v116
	v_ashrrev_i32_e32 v119, 31, v118
	v_ashrrev_i32_e32 v125, 31, v124
	v_ashrrev_i32_e32 v127, 31, v126
	v_ashrrev_i32_e32 v135, 31, v134
	v_ashrrev_i32_e32 v133, 31, v132
	s_ashr_i32 s9, s8, 31
	v_lshlrev_b64 v[110:111], 12, v[110:111]
	v_lshlrev_b64 v[116:117], 12, v[116:117]
	v_lshlrev_b64 v[118:119], 12, v[118:119]
	v_lshlrev_b64 v[124:125], 12, v[124:125]
	v_lshlrev_b64 v[126:127], 12, v[126:127]
	v_lshlrev_b64 v[134:135], 12, v[134:135]
	v_lshlrev_b64 v[132:133], 12, v[132:133]
	v_lshl_add_u64 v[108:109], s[6:7], 0, v[108:109]
	s_lshl_b64 s[8:9], s[8:9], 2
	v_lshl_add_u64 v[110:111], s[6:7], 0, v[110:111]
	v_lshl_add_u64 v[116:117], s[6:7], 0, v[116:117]
	v_lshl_add_u64 v[118:119], s[6:7], 0, v[118:119]
	v_lshl_add_u64 v[124:125], s[6:7], 0, v[124:125]
	v_lshl_add_u64 v[126:127], s[6:7], 0, v[126:127]
	v_lshl_add_u64 v[134:135], s[6:7], 0, v[134:135]
	v_lshl_add_u64 v[132:133], s[6:7], 0, v[132:133]
	v_lshl_add_u64 v[108:109], v[108:109], 0, s[8:9]
	v_lshl_add_u64 v[110:111], v[110:111], 0, s[8:9]
	v_lshl_add_u64 v[116:117], v[116:117], 0, s[8:9]
	v_lshl_add_u64 v[118:119], v[118:119], 0, s[8:9]
	v_lshl_add_u64 v[124:125], v[124:125], 0, s[8:9]
	v_lshl_add_u64 v[126:127], v[126:127], 0, s[8:9]
	v_lshl_add_u64 v[134:135], v[134:135], 0, s[8:9]
	v_lshl_add_u64 v[132:133], v[132:133], 0, s[8:9]
	v_lshl_add_u64 v[108:109], v[108:109], 0, v[56:57]
	v_lshl_add_u64 v[112:113], v[110:111], 0, v[56:57]
	v_lshl_add_u64 v[116:117], v[116:117], 0, v[56:57]
	v_lshl_add_u64 v[120:121], v[118:119], 0, v[56:57]
	v_lshl_add_u64 v[124:125], v[124:125], 0, v[56:57]
	v_lshl_add_u64 v[128:129], v[126:127], 0, v[56:57]
	v_lshl_add_u64 v[134:135], v[134:135], 0, v[56:57]
	v_lshl_add_u64 v[136:137], v[132:133], 0, v[56:57]
	global_load_dwordx4 v[108:111], v[108:109], off nt
	s_nop 0
	global_load_dwordx4 v[112:115], v[112:113], off nt
	s_nop 0
	global_load_dwordx4 v[116:119], v[116:117], off nt
	s_nop 0
	global_load_dwordx4 v[120:123], v[120:121], off nt
	s_nop 0
	global_load_dwordx4 v[124:127], v[124:125], off nt
	s_nop 0
	global_load_dwordx4 v[128:131], v[128:129], off nt
	s_nop 0
	global_load_dwordx4 v[132:135], v[134:135], off nt
	s_nop 0
	global_load_dwordx4 v[136:139], v[136:137], off nt
	v_writelane_b32 v255, s28, 44
	v_writelane_b32 v255, s25, 45
	v_writelane_b32 v255, s4, 46
	v_writelane_b32 v255, s5, 47
	s_add_i32 s22, s22, 8
	s_ashr_i32 s4, s22, 31
	s_lshr_b32 s4, s4, 23
	s_add_i32 s4, s22, s4
	s_ashr_i32 s8, s4, 9
	s_mul_hi_i32 s4, s8, 0x55555556
	s_lshr_b32 s5, s4, 31
	s_add_i32 s4, s4, s5
	s_mul_i32 s4, s4, 3
	s_sub_i32 s9, s8, s4
	s_cmp_eq_u32 s9, 0
	s_cselect_b64 s[6:7], -1, 0
	s_cmp_lg_u32 s9, 0
	s_mov_b64 s[4:5], -1
	s_cbranch_scc0 .Ltkcv_a2_1525
	s_cmp_lg_u32 s9, 1
	s_cbranch_scc0 .Ltkcv_a2_1522
	v_readlane_b32 s4, v255, 5
	s_nop 1
	v_mov_b32_e32 v140, s4
	ds_read_b64 v[140:141], v140
	s_mov_b64 s[4:5], 0
	s_waitcnt lgkmcnt(0)
	v_readfirstlane_b32 s11, v140
	v_readfirstlane_b32 s18, v141
.Ltkcv_a2_1522:
	s_andn2_b64 vcc, exec, s[4:5]
	s_cbranch_vccnz .Ltkcv_a2_1524
	v_readlane_b32 s4, v255, 6
	s_nop 1
	v_mov_b32_e32 v140, s4
	ds_read_b64 v[140:141], v140
	s_waitcnt lgkmcnt(0)
	v_readfirstlane_b32 s11, v140
	v_readfirstlane_b32 s18, v141

; #define GAS __attribute__((address_space(1)))
; __device__ __forceinline__ void titem_load(const TItem& T, int lane, f32x4 (&v)[8]) {
;     const int nblk = T.N / 32, kb = T.item / nblk, nb = T.item % nblk, k0 = 64 * kb, n0 = 32 * nb;
; #pragma unroll
;     for (int i = 0; i < 8; ++i) v[i] = *(const GAS f32x4*)(T.W + (size_t)(k0 + 8 * i + (lane >> 3)) * T.N + n0 + 4 * (lane & 7));
; }
; __device__ __forceinline__ TItem moe_item(Frame& F, int L, int r) {
;     constexpr int I_SQ = 16 * (1024 / 32);
;     const int mi = r / I_SQ, item = r % I_SQ, e = mi / 3, which = mi % 3;
;     const float* W = (which == 0 ? inp(F, I_WG) : which == 1 ? inp(F, I_WU) : inp(F, I_WD)) + (size_t)(L * 16 + e) * 1024 * 1024;
;     bf16_t* WT = (bf16_t*)(which < 2 ? F.ws + WS_WUP + (size_t)(L * 16 + e) * 2048 * 1024 : F.ws + WS_WDN + (size_t)(L * 16 + e) * 1024 * 1024);
;     return TItem{W, WT, 1024, which == 0 ? RM_UPG : which == 1 ? RM_UPU : RM_P8, item, true};
; }
.Ltkcv_a2_1525:
	s_andn2_b64 vcc, exec, s[4:5]
	s_cbranch_vccnz .Ltkcv_a2_1527
	v_readlane_b32 s4, v255, 7
	s_nop 1
	v_mov_b32_e32 v140, s4
	ds_read_b64 v[140:141], v140
	s_waitcnt lgkmcnt(0)
	v_readfirstlane_b32 s11, v140
	v_readfirstlane_b32 s18, v141
.Ltkcv_a2_1527:
	s_mul_hi_i32 s4, s22, 0x2aaaaaab
	s_lshr_b32 s5, s4, 31
	s_ashr_i32 s4, s4, 8
	s_add_i32 s4, s4, s5
	s_add_i32 s28, s4, s17
	s_ashr_i32 s29, s28, 31
	s_lshl_b64 s[4:5], s[28:29], 20
	s_lshl_b64 s[30:31], s[28:29], 21
	v_readlane_b32 s19, v253, 45
	s_add_u32 s19, s19, s30
	v_readlane_b32 s25, v253, 46
	s_addc_u32 s25, s25, s31
	v_readlane_b32 s30, v253, 43
	s_add_u32 s4, s30, s4
	v_readlane_b32 s30, v253, 44
	s_addc_u32 s5, s30, s5
	s_cmp_lt_i32 s9, 2
	s_cselect_b32 s5, s25, s5
	s_cselect_b32 s4, s19, s4
	s_cmp_eq_u32 s9, 1
	s_cselect_b32 s9, 5, 2
	s_and_b64 s[6:7], s[6:7], exec
	s_cselect_b32 s25, 4, s9
	s_lshl_b64 s[6:7], s[28:29], 22
	s_add_u32 s6, s11, s6
	s_addc_u32 s7, s18, s7
	s_lshl_b32 s8, s8, 9
	s_sub_i32 s28, s22, s8
	s_sext_i32_i16 s8, s28
	s_bfe_u32 s8, s8, 0x5001a
	s_add_i32 s8, s28, s8
	s_sext_i32_i16 s9, s8
	s_lshl_b32 s9, s9, 1
	s_andn2_b32 s9, s9, 63
	s_and_b32 s8, s8, 0xffe0
	v_or_b32_e32 v194, s9, v54
	s_sub_i32 s8, s28, s8
	v_ashrrev_i32_e32 v195, 31, v194
	s_sext_i32_i16 s8, s8
	v_lshlrev_b64 v[140:141], 12, v[194:195]
	v_or_b32_e32 v142, 8, v194
	v_or_b32_e32 v156, 16, v194
	v_or_b32_e32 v158, 24, v194
	v_or_b32_e32 v164, 32, v194
	v_or_b32_e32 v166, 40, v194
	v_or_b32_e32 v196, 48, v194
	v_or_b32_e32 v194, 56, v194
	s_lshl_b32 s8, s8, 5
	v_ashrrev_i32_e32 v143, 31, v142
	v_ashrrev_i32_e32 v157, 31, v156
	v_ashrrev_i32_e32 v159, 31, v158
	v_ashrrev_i32_e32 v165, 31, v164
	v_ashrrev_i32_e32 v167, 31, v166
	v_ashrrev_i32_e32 v197, 31, v196
	v_ashrrev_i32_e32 v195, 31, v194
	s_ashr_i32 s9, s8, 31
	v_lshlrev_b64 v[142:143], 12, v[142:143]
	v_lshlrev_b64 v[156:157], 12, v[156:157]
	v_lshlrev_b64 v[158:159], 12, v[158:159]
	v_lshlrev_b64 v[164:165], 12, v[164:165]
	v_lshlrev_b64 v[166:167], 12, v[166:167]
	v_lshlrev_b64 v[196:197], 12, v[196:197]
	v_lshlrev_b64 v[194:195], 12, v[194:195]
	v_lshl_add_u64 v[140:141], s[6:7], 0, v[140:141]
	s_lshl_b64 s[8:9], s[8:9], 2
	v_lshl_add_u64 v[142:143], s[6:7], 0, v[142:143]
	v_lshl_add_u64 v[156:157], s[6:7], 0, v[156:157]
	v_lshl_add_u64 v[158:159], s[6:7], 0, v[158:159]
	v_lshl_add_u64 v[164:165], s[6:7], 0, v[164:165]
	v_lshl_add_u64 v[166:167], s[6:7], 0, v[166:167]
	v_lshl_add_u64 v[196:197], s[6:7], 0, v[196:197]
	v_lshl_add_u64 v[194:195], s[6:7], 0, v[194:195]
	v_lshl_add_u64 v[140:141], v[140:141], 0, s[8:9]
	v_lshl_add_u64 v[142:143], v[142:143], 0, s[8:9]
	v_lshl_add_u64 v[156:157], v[156:157], 0, s[8:9]
	v_lshl_add_u64 v[158:159], v[158:159], 0, s[8:9]
	v_lshl_add_u64 v[164:165], v[164:165], 0, s[8:9]
	v_lshl_add_u64 v[166:167], v[166:167], 0, s[8:9]
	v_lshl_add_u64 v[196:197], v[196:197], 0, s[8:9]
	v_lshl_add_u64 v[194:195], v[194:195], 0, s[8:9]
	v_lshl_add_u64 v[140:141], v[140:141], 0, v[56:57]
	v_lshl_add_u64 v[152:153], v[142:143], 0, v[56:57]
	v_lshl_add_u64 v[156:157], v[156:157], 0, v[56:57]
	v_lshl_add_u64 v[160:161], v[158:159], 0, v[56:57]
	v_lshl_add_u64 v[164:165], v[164:165], 0, v[56:57]
	v_lshl_add_u64 v[168:169], v[166:167], 0, v[56:57]
	v_lshl_add_u64 v[196:197], v[196:197], 0, v[56:57]
	v_lshl_add_u64 v[202:203], v[194:195], 0, v[56:57]
	global_load_dwordx4 v[140:143], v[140:141], off nt
	s_nop 0
	global_load_dwordx4 v[152:155], v[152:153], off nt
	s_nop 0
	global_load_dwordx4 v[156:159], v[156:157], off nt
	s_nop 0
	global_load_dwordx4 v[160:163], v[160:161], off nt
	s_nop 0
	global_load_dwordx4 v[164:167], v[164:165], off nt
	s_nop 0
	global_load_dwordx4 v[168:171], v[168:169], off nt
	s_nop 0
	global_load_dwordx4 v[194:197], v[196:197], off nt
	s_nop 0
	global_load_dwordx4 v[202:205], v[202:203], off nt
	v_writelane_b32 v255, s28, 48
	v_writelane_b32 v255, s25, 49
	v_writelane_b32 v255, s4, 50
	v_writelane_b32 v255, s5, 51
	s_add_i32 s22, s22, 8
	s_ashr_i32 s4, s22, 31
	s_lshr_b32 s4, s4, 23
	s_add_i32 s4, s22, s4
	s_ashr_i32 s8, s4, 9
	s_mul_hi_i32 s4, s8, 0x55555556
	s_lshr_b32 s5, s4, 31
	s_add_i32 s4, s4, s5
	s_mul_i32 s4, s4, 3
	s_sub_i32 s9, s8, s4
	s_cmp_eq_u32 s9, 0
	s_cselect_b64 s[6:7], -1, 0
	s_cmp_lg_u32 s9, 0
	s_mov_b64 s[4:5], -1
	s_cbranch_scc0 .Ltkcv_a3_1525
	s_cmp_lg_u32 s9, 1
	s_cbranch_scc0 .Ltkcv_a3_1522
	v_readlane_b32 s4, v255, 5
	s_nop 1
	v_mov_b32_e32 v214, s4
	ds_read_b64 v[214:215], v214
	s_mov_b64 s[4:5], 0
	s_waitcnt lgkmcnt(0)
	v_readfirstlane_b32 s11, v214
	v_readfirstlane_b32 s18, v215
.Ltkcv_a3_1522:
	s_andn2_b64 vcc, exec, s[4:5]
	s_cbranch_vccnz .Ltkcv_a3_1524
	v_readlane_b32 s4, v255, 6
	s_nop 1
	v_mov_b32_e32 v214, s4
	ds_read_b64 v[214:215], v214
	s_waitcnt lgkmcnt(0)
	v_readfirstlane_b32 s11, v214
	v_readfirstlane_b32 s18, v215

; #define LAS __attribute__((address_space(3)))
; #define PHASE_FRAME(F0) Frame F = F0; { int t_ = threadIdx.x; asm volatile("" : "+v"(t_)); F.tid = t_; F.lane = t_ & 63; F.wave = __builtin_amdgcn_readfirstlane(t_ >> 6); }
; __device__ __forceinline__ TItem moe_item(Frame& F, int L, int r) {
;     constexpr int I_SQ = 16 * (1024 / 32);
;     const int mi = r / I_SQ, item = r % I_SQ, e = mi / 3, which = mi % 3;
;     const float* W = (which == 0 ? inp(F, I_WG) : which == 1 ? inp(F, I_WU) : inp(F, I_WD)) + (size_t)(L * 16 + e) * 1024 * 1024;
;     bf16_t* WT = (bf16_t*)(which < 2 ? F.ws + WS_WUP + (size_t)(L * 16 + e) * 2048 * 1024 : F.ws + WS_WDN + (size_t)(L * 16 + e) * 1024 * 1024);
;     return TItem{W, WT, 1024, which == 0 ? RM_UPG : which == 1 ? RM_UPU : RM_P8, item, true};
; }
; __device__ __forceinline__ void tk_phase(const Frame& F0, bool with_ctx) {
;     PHASE_FRAME(F0);
;     LAS int* cb = (LAS int*)F.lds;
;     const float* AFF = (const float*)(F.ws + WS_AFF);
;     unsigned* IDX = (unsigned*)(F.ws + WS_IDX); float* GATE = (float*)(F.ws + WS_GATE); unsigned short* TOKSLOT = (unsigned short*)(F.ws + WS_TOKSLOT);
;     for (int p = blockIdx.x; p < 256; p += F.G) {
;         const int e = p >> 4, b = p & 15, row0 = b * SEQ, crow0 = NLAT + b * CTXL;
;         const bool cw = with_ctx && F.wave == 0;
;         unsigned key[4], ckey[4];
; #pragma unroll
;         for (int k = 0; k < 4; ++k) { key[k] = __float_as_uint(AFF[(size_t)(row0 + 4 * F.tid + k) * 16 + e]); ckey[k] = cw ? __float_as_uint(AFF[(size_t)(crow0 + 4 * F.lane + k) * 16 + e]) : 0u; }
.Ltkcv_a3_1525:
	s_andn2_b64 vcc, exec, s[4:5]
	s_cbranch_vccnz .Ltkcv_a3_1527
	v_readlane_b32 s4, v255, 7
	s_nop 1
	v_mov_b32_e32 v214, s4
	ds_read_b64 v[214:215], v214
	s_waitcnt lgkmcnt(0)
	v_readfirstlane_b32 s11, v214
	v_readfirstlane_b32 s18, v215
.Ltkcv_a3_1527:
	s_mul_hi_i32 s4, s22, 0x2aaaaaab
	s_lshr_b32 s5, s4, 31
	s_ashr_i32 s4, s4, 8
	s_add_i32 s4, s4, s5
	s_add_i32 s28, s4, s17
	s_ashr_i32 s29, s28, 31
	s_lshl_b64 s[4:5], s[28:29], 20
	s_lshl_b64 s[30:31], s[28:29], 21
	v_readlane_b32 s19, v253, 45
	s_add_u32 s19, s19, s30
	v_readlane_b32 s25, v253, 46
	s_addc_u32 s25, s25, s31
	v_readlane_b32 s30, v253, 43
	s_add_u32 s4, s30, s4
	v_readlane_b32 s30, v253, 44
	s_addc_u32 s5, s30, s5
	s_cmp_lt_i32 s9, 2
	s_cselect_b32 s5, s25, s5
	s_cselect_b32 s4, s19, s4
	s_cmp_eq_u32 s9, 1
	s_cselect_b32 s9, 5, 2
	s_and_b64 s[6:7], s[6:7], exec
	s_cselect_b32 s25, 4, s9
	s_lshl_b64 s[6:7], s[28:29], 22
	s_add_u32 s6, s11, s6
	s_addc_u32 s7, s18, s7
	s_lshl_b32 s8, s8, 9
	s_sub_i32 s28, s22, s8
	s_sext_i32_i16 s8, s28
	s_bfe_u32 s8, s8, 0x5001a
	s_add_i32 s8, s28, s8
	s_sext_i32_i16 s9, s8
	s_lshl_b32 s9, s9, 1
	s_andn2_b32 s9, s9, 63
	s_and_b32 s8, s8, 0xffe0
	v_or_b32_e32 v238, s9, v54
	s_sub_i32 s8, s28, s8
	v_ashrrev_i32_e32 v239, 31, v238
	s_sext_i32_i16 s8, s8
	v_lshlrev_b64 v[214:215], 12, v[238:239]
	v_or_b32_e32 v216, 8, v238
	v_or_b32_e32 v222, 16, v238
	v_or_b32_e32 v224, 24, v238
	v_or_b32_e32 v230, 32, v238
	v_or_b32_e32 v232, 40, v238
	v_or_b32_e32 v240, 48, v238
	v_or_b32_e32 v238, 56, v238
	s_lshl_b32 s8, s8, 5
	v_ashrrev_i32_e32 v217, 31, v216
	v_ashrrev_i32_e32 v223, 31, v222
	v_ashrrev_i32_e32 v225, 31, v224
	v_ashrrev_i32_e32 v231, 31, v230
	v_ashrrev_i32_e32 v233, 31, v232
	v_ashrrev_i32_e32 v241, 31, v240
	v_ashrrev_i32_e32 v239, 31, v238
	s_ashr_i32 s9, s8, 31
	v_lshlrev_b64 v[216:217], 12, v[216:217]
	v_lshlrev_b64 v[222:223], 12, v[222:223]
	v_lshlrev_b64 v[224:225], 12, v[224:225]
	v_lshlrev_b64 v[230:231], 12, v[230:231]
	v_lshlrev_b64 v[232:233], 12, v[232:233]
	v_lshlrev_b64 v[240:241], 12, v[240:241]
	v_lshlrev_b64 v[238:239], 12, v[238:239]
	v_lshl_add_u64 v[214:215], s[6:7], 0, v[214:215]
	s_lshl_b64 s[8:9], s[8:9], 2
	v_lshl_add_u64 v[216:217], s[6:7], 0, v[216:217]
	v_lshl_add_u64 v[222:223], s[6:7], 0, v[222:223]
	v_lshl_add_u64 v[224:225], s[6:7], 0, v[224:225]
	v_lshl_add_u64 v[230:231], s[6:7], 0, v[230:231]
	v_lshl_add_u64 v[232:233], s[6:7], 0, v[232:233]
	v_lshl_add_u64 v[240:241], s[6:7], 0, v[240:241]
	v_lshl_add_u64 v[238:239], s[6:7], 0, v[238:239]
	v_lshl_add_u64 v[214:215], v[214:215], 0, s[8:9]
	v_lshl_add_u64 v[216:217], v[216:217], 0, s[8:9]
	v_lshl_add_u64 v[222:223], v[222:223], 0, s[8:9]
	v_lshl_add_u64 v[224:225], v[224:225], 0, s[8:9]
	v_lshl_add_u64 v[230:231], v[230:231], 0, s[8:9]
	v_lshl_add_u64 v[232:233], v[232:233], 0, s[8:9]
	v_lshl_add_u64 v[240:241], v[240:241], 0, s[8:9]
	v_lshl_add_u64 v[238:239], v[238:239], 0, s[8:9]
	v_lshl_add_u64 v[214:215], v[214:215], 0, v[56:57]
	v_lshl_add_u64 v[218:219], v[216:217], 0, v[56:57]
	v_lshl_add_u64 v[222:223], v[222:223], 0, v[56:57]
	v_lshl_add_u64 v[226:227], v[224:225], 0, v[56:57]
	v_lshl_add_u64 v[230:231], v[230:231], 0, v[56:57]
	v_lshl_add_u64 v[234:235], v[232:233], 0, v[56:57]
	v_lshl_add_u64 v[240:241], v[240:241], 0, v[56:57]
	v_lshl_add_u64 v[242:243], v[238:239], 0, v[56:57]
	global_load_dwordx4 v[214:217], v[214:215], off nt
	s_nop 0
	global_load_dwordx4 v[218:221], v[218:219], off nt
	s_nop 0
	global_load_dwordx4 v[222:225], v[222:223], off nt
	s_nop 0
	global_load_dwordx4 v[226:229], v[226:227], off nt
	s_nop 0
	global_load_dwordx4 v[230:233], v[230:231], off nt
	s_nop 0
	global_load_dwordx4 v[234:237], v[234:235], off nt
	s_nop 0
	global_load_dwordx4 v[238:241], v[240:241], off nt
	s_nop 0
	global_load_dwordx4 v[242:245], v[242:243], off nt
	v_writelane_b32 v255, s28, 52
	v_writelane_b32 v255, s25, 53
	v_writelane_b32 v255, s4, 54
	v_writelane_b32 v255, s5, 55
	s_mov_b32 s4, 1
	v_writelane_b32 v255, s4, 56
.Ltkcv_a_done:
	v_readfirstlane_b32 s0, v1
	s_nop 3
	s_ashr_i32 s12, s0, 6
	s_cmp_lt_u32 s0, 64
	v_readlane_b32 s2, v255, 14
	s_cselect_b64 s[0:1], -1, 0
	v_readlane_b32 s3, v255, 15
	s_and_b64 s[2:3], s[2:3], s[0:1]
	s_lshl_b32 s0, s12, 2
	s_add_i32 s17, s0, 0
	s_cmp_gt_i32 s12, 0
	s_cselect_b64 s[4:5], -1, 0
	s_cmp_gt_u32 s12, 3
	s_waitcnt lgkmcnt(0)
	v_and_b32_e32 v2, 63, v1
	s_cselect_b64 s[6:7], -1, 0
	s_and_b32 s25, s12, 0x7ffffffc
	v_lshlrev_b32_e32 v10, 2, v1
	v_lshlrev_b32_e32 v12, 2, v2
	v_cmp_eq_u32_e64 s[36:37], 0, v2
	v_lshlrev_b64 v[2:3], v1, -1
	s_cmp_lg_u32 s12, s25
	v_not_b32_e32 v1, v3
	v_not_b32_e32 v14, v2
	v_or_b32_e32 v13, 1, v12
	v_or_b32_e32 v15, 2, v12
	v_or_b32_e32 v22, 3, v12
	v_ashrrev_i32_e32 v11, 31, v10
	v_or_b32_e32 v23, 1, v10
	v_or_b32_e32 v24, 2, v10
	v_or_b32_e32 v25, 3, v10
	s_cselect_b64 s[8:9], -1, 0
	s_mov_b32 s10, s84
	s_branch .LBB0_1274

; #define LAS __attribute__((address_space(3)))
; #define LDS_WAIT() asm volatile("s_waitcnt lgkmcnt(0)" ::: "memory")
; __device__ __forceinline__ void titem_store(const TItem& T, int lane, const f32x4 (&v)[8], LAS float* scr) {
;     const int nblk = T.N / 32, kb = T.item / nblk, nb = T.item % nblk, k0 = 64 * kb, n0 = 32 * nb;
; #pragma unroll
;     for (int i = 0; i < 8; ++i) { LAS float* s = scr + (8 * i + (lane >> 3)) * 33 + 4 * (lane & 7); s[0] = v[i][0]; s[1] = v[i][1]; s[2] = v[i][2]; s[3] = v[i][3]; }
;     LDS_WAIT(); asm volatile("" ::: "memory");
;     const int c = lane & 7;
; #pragma unroll
;     for (int j = 0; j < 4; ++j) { const int n = (lane >> 3) + 8 * j; const LAS float* s = scr + (8 * c) * 33 + n;
; __device__ __forceinline__ void moe_convert_run(Frame& F, int L, int first, int end, int stride, LAS float* scr) {
;     if (first >= end) return;
;     f32x4 nv[8]; TItem nT = moe_item(F, L, first); titem_load(nT, F.lane, nv);
;     for (int r = first; r < end; r += stride) {
;         const TItem T = nT; f32x4 v[8];
; #pragma unroll
;         for (int i = 0; i < 8; ++i) v[i] = nv[i];
;         if (r + stride < end) { nT = moe_item(F, L, r + stride); titem_load(nT, F.lane, nv); }
;         titem_store(T, F.lane, v, scr);
;     }
; }
.LBB0_1334:
	v_readlane_b32 s4, v255, 56
	s_cmp_eq_u32 s4, 0
	s_cbranch_scc1 .Ltkcv_b_done
	s_mov_b32 s4, 0
	v_writelane_b32 v255, s4, 56
	v_mov_b32_e32 v2, v0
	v_readfirstlane_b32 s4, v2
	s_nop 3
	s_ashr_i32 s4, s4, 6
	s_lshl_b32 s4, s4, 14
	s_add_i32 s11, s4, 0
	v_bfe_u32 v1, v2, 3, 3
	v_lshlrev_b32_e32 v3, 2, v2
	v_and_b32_e32 v8, 28, v3
	v_lshlrev_b32_e32 v190, 2, v8
	v_lshlrev_b32_e32 v5, 3, v2
	v_and_b32_e32 v66, 56, v5
	v_add_u32_e32 v3, s11, v190
	v_mul_u32_u24_e32 v4, 0x84, v1
	v_mul_u32_u24_e32 v5, 0x84, v66
	v_bfe_u32 v68, v2, 3, 2
	v_lshlrev_b32_e32 v2, 2, v1
	v_add3_u32 v69, s11, v5, v2
	v_and_b32_e32 v70, 16, v2
	v_or_b32_e32 v73, 12, v2
	v_lshlrev_b32_e32 v190, 2, v8
	v_add_u32_e32 v74, v3, v4
	v_mov_b32_e32 v67, v191
	v_or_b32_e32 v71, 4, v70
	v_or_b32_e32 v72, 8, v70
	s_waitcnt vmcnt(0)
	s_mov_b32 s22, 0
	s_branch .Ltkcv_b_done
.Ltkcv_loop:
	s_cmp_eq_u32 s22, 0
	s_cbranch_scc0 .Ltkcv_sel1
	v_mov_b64_e32 v[36:37], v[106:107]
	v_mov_b64_e32 v[40:41], v[102:103]
	v_mov_b64_e32 v[44:45], v[98:99]
	v_mov_b64_e32 v[48:49], v[94:95]
	v_mov_b64_e32 v[52:53], v[90:91]
	v_mov_b64_e32 v[56:57], v[86:87]
	v_mov_b64_e32 v[60:61], v[82:83]
	v_mov_b64_e32 v[64:65], v[78:79]
	v_mov_b64_e32 v[34:35], v[104:105]
	v_mov_b64_e32 v[38:39], v[100:101]
	v_mov_b64_e32 v[42:43], v[96:97]
	v_mov_b64_e32 v[46:47], v[92:93]
	v_mov_b64_e32 v[50:51], v[88:89]
	v_mov_b64_e32 v[54:55], v[84:85]
	v_mov_b64_e32 v[58:59], v[80:81]
	v_mov_b64_e32 v[62:63], v[76:77]
	v_readlane_b32 s10, v255, 40
	v_readlane_b32 s23, v255, 41
	v_readlane_b32 s0, v255, 42
	v_readlane_b32 s1, v255, 43
	s_branch .Ltkcv_go
.Ltkcv_sel1:
	s_cmp_eq_u32 s22, 1
	s_cbranch_scc0 .Ltkcv_sel2
	v_mov_b64_e32 v[36:37], v[138:139]
	v_mov_b64_e32 v[40:41], v[134:135]
	v_mov_b64_e32 v[44:45], v[130:131]
	v_mov_b64_e32 v[48:49], v[126:127]
	v_mov_b64_e32 v[52:53], v[122:123]
	v_mov_b64_e32 v[56:57], v[118:119]
	v_mov_b64_e32 v[60:61], v[114:115]
	v_mov_b64_e32 v[64:65], v[110:111]
	v_mov_b64_e32 v[34:35], v[136:137]
	v_mov_b64_e32 v[38:39], v[132:133]
	v_mov_b64_e32 v[42:43], v[128:129]
	v_mov_b64_e32 v[46:47], v[124:125]
	v_mov_b64_e32 v[50:51], v[120:121]
	v_mov_b64_e32 v[54:55], v[116:117]
	v_mov_b64_e32 v[58:59], v[112:113]
	v_mov_b64_e32 v[62:63], v[108:109]
	v_readlane_b32 s10, v255, 44
	v_readlane_b32 s23, v255, 45
	v_readlane_b32 s0, v255, 46
	v_readlane_b32 s1, v255, 47
	s_branch .Ltkcv_go
.Ltkcv_sel2:
	s_cmp_eq_u32 s22, 2
	s_cbranch_scc0 .Ltkcv_sel3
	v_mov_b64_e32 v[36:37], v[204:205]
	v_mov_b64_e32 v[40:41], v[196:197]
	v_mov_b64_e32 v[44:45], v[170:171]
	v_mov_b64_e32 v[48:49], v[166:167]
	v_mov_b64_e32 v[52:53], v[162:163]
	v_mov_b64_e32 v[56:57], v[158:159]
	v_mov_b64_e32 v[60:61], v[154:155]
	v_mov_b64_e32 v[64:65], v[142:143]
	v_mov_b64_e32 v[34:35], v[202:203]
	v_mov_b64_e32 v[38:39], v[194:195]
	v_mov_b64_e32 v[42:43], v[168:169]
	v_mov_b64_e32 v[46:47], v[164:165]
	v_mov_b64_e32 v[50:51], v[160:161]
	v_mov_b64_e32 v[54:55], v[156:157]
	v_mov_b64_e32 v[58:59], v[152:153]
	v_mov_b64_e32 v[62:63], v[140:141]
	v_readlane_b32 s10, v255, 48
	v_readlane_b32 s23, v255, 49
	v_readlane_b32 s0, v255, 50
	v_readlane_b32 s1, v255, 51
	s_branch .Ltkcv_go
.Ltkcv_sel3:
	v_mov_b64_e32 v[36:37], v[244:245]
	v_mov_b64_e32 v[40:41], v[240:241]
	v_mov_b64_e32 v[44:45], v[236:237]
	v_mov_b64_e32 v[48:49], v[232:233]
	v_mov_b64_e32 v[52:53], v[228:229]
	v_mov_b64_e32 v[56:57], v[224:225]
	v_mov_b64_e32 v[60:61], v[220:221]
	v_mov_b64_e32 v[64:65], v[216:217]
	v_mov_b64_e32 v[34:35], v[242:243]
	v_mov_b64_e32 v[38:39], v[238:239]
	v_mov_b64_e32 v[42:43], v[234:235]
	v_mov_b64_e32 v[46:47], v[230:231]
	v_mov_b64_e32 v[50:51], v[226:227]
	v_mov_b64_e32 v[54:55], v[222:223]
	v_mov_b64_e32 v[58:59], v[218:219]
	v_mov_b64_e32 v[62:63], v[214:215]
	v_readlane_b32 s10, v255, 52
	v_readlane_b32 s23, v255, 53
	v_readlane_b32 s0, v255, 54
	v_readlane_b32 s1, v255, 55

; #define GAS __attribute__((address_space(1)))
; #define LAS __attribute__((address_space(3)))
; #define LDS_WAIT() asm volatile("s_waitcnt lgkmcnt(0)" ::: "memory")
; __device__ __forceinline__ unsigned pk2(float lo, float hi) { unsigned r; asm("v_cvt_pk_bf16_f32 %0, %1, %2" : "=v"(r) : "v"(lo), "v"(hi)); return r; }
; #define PHASE_FRAME(F0) Frame F = F0; { int t_ = threadIdx.x; asm volatile("" : "+v"(t_)); F.tid = t_; F.lane = t_ & 63; F.wave = __builtin_amdgcn_readfirstlane(t_ >> 6); }
; __device__ __forceinline__ void titem_store(const TItem& T, int lane, const f32x4 (&v)[8], LAS float* scr) {
;     ...
;     for (int j = 0; j < 4; ++j) { const int n = (lane >> 3) + 8 * j; const LAS float* s = scr + (8 * c) * 33 + n;
;         if (T.f8) { u32x2 o; o.x = pg8::pack4_fp8(s[0 * 33] * pg8::SC_W, s[1 * 33] * pg8::SC_W, s[2 * 33] * pg8::SC_W, s[3 * 33] * pg8::SC_W); o.y = pg8::pack4_fp8(s[4 * 33] * pg8::SC_W, s[5 * 33] * pg8::SC_W, s[6 * 33] * pg8::SC_W, s[7 * 33] * pg8::SC_W);
;             *(GAS u32x2*)((unsigned char*)T.WT + (size_t)row_map(T.mode, n0, n) * 1024 + k0 + 8 * c) = o; }
;         else { u32x4 o; o.x = pk2(s[0 * 33], s[1 * 33]); o.y = pk2(s[2 * 33], s[3 * 33]); o.z = pk2(s[4 * 33], s[5 * 33]); o.w = pk2(s[6 * 33], s[7 * 33]);
;             *(GAS u32x4*)(T.WT + (size_t)row_map(T.mode, n0, n) * 1024 + k0 + 8 * c) = o; } }
;     LDS_WAIT(); asm volatile("" ::: "memory");
; }
; __device__ __forceinline__ void moe_convert_slice(const Frame& F0, int L, int first, int n, int rank, int n_idle) {
;     PHASE_FRAME(F0);
;     const int per = (n + n_idle - 1) / n_idle, lo = first + rank * per, hi = (lo + per < first + n) ? lo + per : first + n;
;     moe_convert_run(F, L, lo + F.wave, hi, 8, (LAS float*)(F.lds + F.wave * 16384));
; }
.Ltkcv_b_1517:
	s_waitcnt lgkmcnt(3)
	v_mul_f32_e32 v40, 0x43800000, v40
	v_mul_f32_e32 v41, 0x43800000, v41
	s_waitcnt lgkmcnt(2)
	v_mul_f32_e32 v43, 0x43800000, v38
	v_med3_f32 v40, v40, s15, v212
	v_med3_f32 v41, v41, s15, v212
	v_mov_b32_e32 v38, v191
	v_cvt_pk_fp8_f32 v38, v40, v41
	v_mul_f32_e32 v39, 0x43800000, v39
	v_med3_f32 v40, v43, s15, v212
	v_med3_f32 v39, v39, s15, v212
	s_waitcnt lgkmcnt(1)
	v_mul_f32_e32 v36, 0x43800000, v36
	v_mul_f32_e32 v37, 0x43800000, v37
	v_cvt_pk_fp8_f32 v38, v40, v39 op_sel:[0,0,1]
	v_med3_f32 v36, v36, s15, v212
	v_med3_f32 v37, v37, s15, v212
	v_mov_b32_e32 v39, v191
	v_cvt_pk_fp8_f32 v39, v36, v37
	s_waitcnt lgkmcnt(0)
	v_mul_f32_e32 v34, 0x43800000, v34
	v_mul_f32_e32 v35, 0x43800000, v35
	v_med3_f32 v34, v34, s15, v212
	v_med3_f32 v35, v35, s15, v212
	v_cvt_pk_fp8_f32 v39, v34, v35 op_sel:[0,0,1]
	v_or_b32_e32 v34, v42, v73
	v_ashrrev_i32_e32 v35, 31, v34
	v_lshlrev_b64 v[34:35], 10, v[34:35]
	v_lshl_add_u64 v[34:35], s[0:1], 0, v[34:35]
	v_lshl_add_u64 v[34:35], v[34:35], 0, s[6:7]
	v_lshl_add_u64 v[34:35], v[34:35], 0, v[66:67]
	global_store_dwordx2 v[34:35], v[38:39], off nt
	s_waitcnt lgkmcnt(0)
	s_add_i32 s22, s22, 1
	s_cmp_lt_u32 s22, 4
	s_cbranch_scc1 .Ltkcv_loop
.Ltkcv_b_done:
	v_readlane_b32 s0, v255, 17
	s_cmp_eq_u32 s0, 3
	s_cbranch_scc1 .Ltkser_done
	s_mov_b32 s30, 1
	v_writelane_b32 v255, s30, 57
	v_readlane_b32 s0, v255, 17
	v_readlane_b32 s1, v255, 18
	s_add_i32 s6, s0, 1
	s_mov_b32 s2, s0
	s_cmp_eq_u32 s6, 2
	s_movk_i32 s0, 0x1c00
	s_movk_i32 s1, 0x2000
	s_cselect_b32 s0, 0x1000, s0
	s_cselect_b32 s1, 0x2000, s1
	s_cmp_eq_u32 s2, 0
	v_mov_b32_e32 v2, v0
	s_cselect_b32 s1, 0x2000, s1
	s_cselect_b32 s0, 0x1600, s0
	v_readfirstlane_b32 s2, v2
	s_ashr_i32 s8, s2, 6
	s_lshr_b32 s2, s1, 8
	s_mov_b32 s3, s84
	s_mul_i32 s3, s2, s3
	s_add_i32 s3, s3, s0
	s_add_i32 s2, s3, s2
	s_add_i32 s1, s1, s0
	s_min_i32 s12, s2, s1
	s_add_i32 s4, s8, s3
	s_cmp_ge_i32 s4, s12
	s_cbranch_scc1 .Ltkser_done
	s_ashr_i32 s0, s4, 31
	s_lshr_b32 s0, s0, 23
	s_add_i32 s0, s4, s0
	s_ashr_i32 s7, s0, 9
	s_mul_hi_i32 s0, s7, 0x55555556
	s_lshr_b32 s1, s0, 31
	s_add_i32 s0, s0, s1
	s_mul_i32 s0, s0, 3
	s_sub_i32 s5, s7, s0
	s_cmp_eq_u32 s5, 0
	s_cselect_b64 s[2:3], -1, 0
	s_cmp_lg_u32 s5, 0
	s_mov_b64 s[0:1], -1
	s_cbranch_scc0 .Ltkser_1514
	s_cmp_lg_u32 s5, 1
	s_cbranch_scc0 .Ltkser_1511
	v_readlane_b32 s0, v255, 5
	s_nop 1
	v_mov_b32_e32 v1, s0
	ds_read_b64 v[4:5], v1
	s_mov_b64 s[0:1], 0
	s_waitcnt lgkmcnt(0)
	v_readfirstlane_b32 s9, v4
	v_readfirstlane_b32 s10, v5

; #define LAS __attribute__((address_space(3)))
; __device__ __forceinline__ TItem moe_item(Frame& F, int L, int r) {
;     constexpr int I_SQ = 16 * (1024 / 32);
;     const int mi = r / I_SQ, item = r % I_SQ, e = mi / 3, which = mi % 3;
;     const float* W = (which == 0 ? inp(F, I_WG) : which == 1 ? inp(F, I_WU) : inp(F, I_WD)) + (size_t)(L * 16 + e) * 1024 * 1024;
;     bf16_t* WT = (bf16_t*)(which < 2 ? F.ws + WS_WUP + (size_t)(L * 16 + e) * 2048 * 1024 : F.ws + WS_WDN + (size_t)(L * 16 + e) * 1024 * 1024);
;     return TItem{W, WT, 1024, which == 0 ? RM_UPG : which == 1 ? RM_UPU : RM_P8, item, true};
; }
; __device__ __forceinline__ void moe_convert_run(Frame& F, int L, int first, int end, int stride, LAS float* scr) {
;     if (first >= end) return;
;     f32x4 nv[8]; TItem nT = moe_item(F, L, first); titem_load(nT, F.lane, nv);
;     for (int r = first; r < end; r += stride) {
;         const TItem T = nT; f32x4 v[8];
; #pragma unroll
;         for (int i = 0; i < 8; ++i) v[i] = nv[i];
;         if (r + stride < end) { nT = moe_item(F, L, r + stride); titem_load(nT, F.lane, nv); }
;         titem_store(T, F.lane, v, scr);
;     }
; }
.Ltkser_1516:
	s_mul_hi_i32 s0, s4, 0x2aaaaaab
	s_lshr_b32 s1, s0, 31
	s_ashr_i32 s0, s0, 8
	s_add_i32 s0, s0, s1
	s_lshl_b32 s17, s6, 4
	s_add_i32 s18, s0, s17
	s_lshl_b32 s1, s8, 14
	s_ashr_i32 s19, s18, 31
	s_add_i32 s11, s1, 0
	s_lshl_b64 s[0:1], s[18:19], 20
	s_lshl_b64 s[22:23], s[18:19], 21
	v_readlane_b32 s6, v253, 45
	s_add_u32 s6, s6, s22
	v_readlane_b32 s8, v253, 46
	s_addc_u32 s8, s8, s23
	v_readlane_b32 s22, v253, 43
	s_add_u32 s0, s22, s0
	v_readlane_b32 s22, v253, 44
	s_addc_u32 s1, s22, s1
	s_cmp_lt_i32 s5, 2
	s_cselect_b32 s1, s8, s1
	s_cselect_b32 s0, s6, s0
	s_lshl_b64 s[18:19], s[18:19], 22
	s_add_u32 s8, s9, s18
	s_addc_u32 s9, s10, s19
	s_lshl_b32 s6, s7, 9
	s_sub_i32 s10, s4, s6
	s_bfe_u32 s6, s10, 0x5001a
	s_add_i32 s6, s10, s6
	s_sext_i32_i16 s7, s6
	s_lshl_b32 s7, s7, 1
	v_bfe_u32 v1, v2, 3, 3
	s_andn2_b32 s7, s7, 63
	s_and_b32 s6, s6, 0xffe0
	v_or_b32_e32 v4, s7, v1
	s_sub_i32 s6, s10, s6
	s_sext_i32_i16 s6, s6
	v_or_b32_e32 v20, 8, v4
	s_lshl_b32 s6, s6, 5
	v_or_b32_e32 v10, 48, v4
	v_or_b32_e32 v12, 40, v4
	v_or_b32_e32 v14, 32, v4
	v_or_b32_e32 v16, 24, v4
	v_or_b32_e32 v18, 16, v4
	v_ashrrev_i32_e32 v21, 31, v20
	v_ashrrev_i32_e32 v5, 31, v4
	v_or_b32_e32 v6, 56, v4
	s_ashr_i32 s7, s6, 31
	v_lshlrev_b32_e32 v3, 2, v2
	v_ashrrev_i32_e32 v11, 31, v10
	v_ashrrev_i32_e32 v13, 31, v12
	v_ashrrev_i32_e32 v15, 31, v14
	v_ashrrev_i32_e32 v17, 31, v16
	v_ashrrev_i32_e32 v19, 31, v18
	v_lshlrev_b64 v[20:21], 12, v[20:21]
	v_lshlrev_b64 v[4:5], 12, v[4:5]
	v_ashrrev_i32_e32 v7, 31, v6
	s_lshl_b64 s[6:7], s[6:7], 2
	v_and_b32_e32 v8, 28, v3
	v_lshlrev_b64 v[10:11], 12, v[10:11]
	v_lshlrev_b64 v[12:13], 12, v[12:13]
	v_lshlrev_b64 v[14:15], 12, v[14:15]
	v_lshlrev_b64 v[16:17], 12, v[16:17]
	v_lshlrev_b64 v[18:19], 12, v[18:19]
	v_lshl_add_u64 v[20:21], s[8:9], 0, v[20:21]
	v_lshl_add_u64 v[4:5], s[8:9], 0, v[4:5]
	v_lshlrev_b64 v[6:7], 12, v[6:7]
	v_lshlrev_b32_e32 v190, 2, v8
	v_lshl_add_u64 v[10:11], s[8:9], 0, v[10:11]
	v_lshl_add_u64 v[12:13], s[8:9], 0, v[12:13]
	v_lshl_add_u64 v[14:15], s[8:9], 0, v[14:15]
	v_lshl_add_u64 v[16:17], s[8:9], 0, v[16:17]
	v_lshl_add_u64 v[18:19], s[8:9], 0, v[18:19]
	v_lshl_add_u64 v[20:21], v[20:21], 0, s[6:7]
	v_lshl_add_u64 v[4:5], v[4:5], 0, s[6:7]
	v_lshl_add_u64 v[6:7], s[8:9], 0, v[6:7]
	v_lshl_add_u64 v[10:11], v[10:11], 0, s[6:7]
	v_lshl_add_u64 v[12:13], v[12:13], 0, s[6:7]
	v_lshl_add_u64 v[14:15], v[14:15], 0, s[6:7]
	v_lshl_add_u64 v[16:17], v[16:17], 0, s[6:7]
	v_lshl_add_u64 v[18:19], v[18:19], 0, s[6:7]
	v_lshl_add_u64 v[20:21], v[20:21], 0, v[190:191]
	v_lshl_add_u64 v[4:5], v[4:5], 0, v[190:191]
	v_lshl_add_u64 v[6:7], v[6:7], 0, s[6:7]
	v_lshl_add_u64 v[12:13], v[12:13], 0, v[190:191]
	v_lshl_add_u64 v[14:15], v[14:15], 0, v[190:191]
	v_lshl_add_u64 v[16:17], v[16:17], 0, v[190:191]
	v_lshl_add_u64 v[18:19], v[18:19], 0, v[190:191]
	s_waitcnt vmcnt(0)
	v_mov_b64_e32 v[58:59], v[80:81]
	v_mov_b64_e32 v[60:61], v[82:83]
	v_mov_b64_e32 v[62:63], v[76:77]
	v_mov_b64_e32 v[64:65], v[78:79]
	v_mov_b64_e32 v[50:51], v[88:89]
	v_mov_b64_e32 v[52:53], v[90:91]
	v_mov_b64_e32 v[54:55], v[84:85]
	v_mov_b64_e32 v[56:57], v[86:87]
	v_mov_b64_e32 v[42:43], v[96:97]
	v_mov_b64_e32 v[44:45], v[98:99]
	v_mov_b64_e32 v[46:47], v[92:93]
	v_mov_b64_e32 v[48:49], v[94:95]
	v_lshl_add_u64 v[4:5], v[10:11], 0, v[190:191]
	v_lshl_add_u64 v[6:7], v[6:7], 0, v[190:191]
	v_mov_b64_e32 v[38:39], v[100:101]
	v_mov_b64_e32 v[40:41], v[102:103]
	v_mov_b64_e32 v[34:35], v[104:105]
	v_mov_b64_e32 v[36:37], v[106:107]
	v_lshlrev_b32_e32 v5, 3, v2
	s_cmp_eq_u32 s5, 1
	v_and_b32_e32 v66, 56, v5
	s_cselect_b32 s5, 5, 2
	s_and_b64 s[2:3], s[2:3], exec
	v_add_u32_e32 v3, s11, v190
	v_mul_u32_u24_e32 v4, 0x84, v1
	v_mul_u32_u24_e32 v5, 0x84, v66
	v_bfe_u32 v68, v2, 3, 2
	v_lshlrev_b32_e32 v2, 2, v1
	s_cselect_b32 s23, 4, s5
	v_add3_u32 v69, s11, v5, v2
	v_and_b32_e32 v70, 16, v2
	v_or_b32_e32 v73, 12, v2
	v_lshlrev_b32_e32 v190, 2, v8
	v_add_u32_e32 v74, v3, v4
	v_mov_b32_e32 v67, v191
	v_or_b32_e32 v71, 4, v70
	v_or_b32_e32 v72, 8, v70
	s_add_i32 s22, s4, 8
	s_mov_b32 s28, s10
	s_mov_b32 s25, s23
	s_mov_b64 s[4:5], s[0:1]
	s_waitcnt vmcnt(7)
	v_mov_b64_e32 v[6:7], v[58:59]
	s_waitcnt vmcnt(6)
	v_mov_b64_e32 v[2:3], v[62:63]
	s_waitcnt vmcnt(5)
	v_mov_b64_e32 v[14:15], v[50:51]
	s_waitcnt vmcnt(4)
	v_mov_b64_e32 v[10:11], v[54:55]
	s_waitcnt vmcnt(3)
	v_mov_b64_e32 v[22:23], v[42:43]
	s_waitcnt vmcnt(2)
	v_mov_b64_e32 v[18:19], v[46:47]
	v_mov_b64_e32 v[4:5], v[64:65]
	s_waitcnt vmcnt(1)
	v_mov_b64_e32 v[26:27], v[38:39]
	s_waitcnt vmcnt(0)
	v_mov_b64_e32 v[30:31], v[34:35]
	v_mov_b64_e32 v[8:9], v[60:61]
	v_mov_b64_e32 v[12:13], v[56:57]
	v_mov_b64_e32 v[16:17], v[52:53]
	v_mov_b64_e32 v[20:21], v[48:49]
	v_mov_b64_e32 v[24:25], v[44:45]
	v_mov_b64_e32 v[28:29], v[40:41]
	v_mov_b64_e32 v[32:33], v[36:37]
	s_branch .Ltkser_1518

; #define GAS __attribute__((address_space(1)))
; __device__ __forceinline__ void titem_load(const TItem& T, int lane, f32x4 (&v)[8]) {
;     const int nblk = T.N / 32, kb = T.item / nblk, nb = T.item % nblk, k0 = 64 * kb, n0 = 32 * nb;
; #pragma unroll
;     for (int i = 0; i < 8; ++i) v[i] = *(const GAS f32x4*)(T.W + (size_t)(k0 + 8 * i + (lane >> 3)) * T.N + n0 + 4 * (lane & 7));
; }
; __device__ __forceinline__ void moe_convert_run(Frame& F, int L, int first, int end, int stride, LAS float* scr) {
;     ...
;     for (int r = first; r < end; r += stride) {
;         const TItem T = nT; f32x4 v[8];
; #pragma unroll
;         for (int i = 0; i < 8; ++i) v[i] = nv[i];
;         if (r + stride < end) { nT = moe_item(F, L, r + stride); titem_load(nT, F.lane, nv); }
;         titem_store(T, F.lane, v, scr);
;     }
.Ltkser_1527:
	s_mul_hi_i32 s4, s22, 0x2aaaaaab
	s_lshr_b32 s5, s4, 31
	s_ashr_i32 s4, s4, 8
	s_add_i32 s4, s4, s5
	s_add_i32 s28, s4, s17
	s_ashr_i32 s29, s28, 31
	s_lshl_b64 s[4:5], s[28:29], 20
	s_lshl_b64 s[30:31], s[28:29], 21
	v_readlane_b32 s19, v253, 45
	s_add_u32 s19, s19, s30
	v_readlane_b32 s25, v253, 46
	s_addc_u32 s25, s25, s31
	v_readlane_b32 s30, v253, 43
	s_add_u32 s4, s30, s4
	v_readlane_b32 s30, v253, 44
	s_addc_u32 s5, s30, s5
	s_cmp_lt_i32 s9, 2
	s_cselect_b32 s5, s25, s5
	s_cselect_b32 s4, s19, s4
	s_cmp_eq_u32 s9, 1
	s_cselect_b32 s9, 5, 2
	s_and_b64 s[6:7], s[6:7], exec
	s_cselect_b32 s25, 4, s9
	s_lshl_b64 s[6:7], s[28:29], 22
	s_add_u32 s6, s11, s6
	s_addc_u32 s7, s18, s7
	s_lshl_b32 s8, s8, 9
	s_sub_i32 s28, s22, s8
	s_sext_i32_i16 s8, s28
	s_bfe_u32 s8, s8, 0x5001a
	s_add_i32 s8, s28, s8
	s_sext_i32_i16 s9, s8
	s_lshl_b32 s9, s9, 1
	s_andn2_b32 s9, s9, 63
	s_and_b32 s8, s8, 0xffe0
	v_or_b32_e32 v26, s9, v1
	s_sub_i32 s8, s28, s8
	v_ashrrev_i32_e32 v27, 31, v26
	s_sext_i32_i16 s8, s8
	v_lshlrev_b64 v[2:3], 12, v[26:27]
	v_or_b32_e32 v4, 8, v26
	v_or_b32_e32 v10, 16, v26
	v_or_b32_e32 v12, 24, v26
	v_or_b32_e32 v18, 32, v26
	v_or_b32_e32 v20, 40, v26
	v_or_b32_e32 v28, 48, v26
	v_or_b32_e32 v26, 56, v26
	s_lshl_b32 s8, s8, 5
	v_ashrrev_i32_e32 v5, 31, v4
	v_ashrrev_i32_e32 v11, 31, v10
	v_ashrrev_i32_e32 v13, 31, v12
	v_ashrrev_i32_e32 v19, 31, v18
	v_ashrrev_i32_e32 v21, 31, v20
	v_ashrrev_i32_e32 v29, 31, v28
	v_ashrrev_i32_e32 v27, 31, v26
	s_ashr_i32 s9, s8, 31
	v_lshlrev_b64 v[4:5], 12, v[4:5]
	v_lshlrev_b64 v[10:11], 12, v[10:11]
	v_lshlrev_b64 v[12:13], 12, v[12:13]
	v_lshlrev_b64 v[18:19], 12, v[18:19]
	v_lshlrev_b64 v[20:21], 12, v[20:21]
	v_lshlrev_b64 v[28:29], 12, v[28:29]
	v_lshlrev_b64 v[26:27], 12, v[26:27]
	v_lshl_add_u64 v[2:3], s[6:7], 0, v[2:3]
	s_lshl_b64 s[8:9], s[8:9], 2
	v_lshl_add_u64 v[4:5], s[6:7], 0, v[4:5]
	v_lshl_add_u64 v[10:11], s[6:7], 0, v[10:11]
	v_lshl_add_u64 v[12:13], s[6:7], 0, v[12:13]
	v_lshl_add_u64 v[18:19], s[6:7], 0, v[18:19]
	v_lshl_add_u64 v[20:21], s[6:7], 0, v[20:21]
	v_lshl_add_u64 v[28:29], s[6:7], 0, v[28:29]
	v_lshl_add_u64 v[26:27], s[6:7], 0, v[26:27]
	v_lshl_add_u64 v[2:3], v[2:3], 0, s[8:9]
	v_lshl_add_u64 v[4:5], v[4:5], 0, s[8:9]
	v_lshl_add_u64 v[10:11], v[10:11], 0, s[8:9]
	v_lshl_add_u64 v[12:13], v[12:13], 0, s[8:9]
	v_lshl_add_u64 v[18:19], v[18:19], 0, s[8:9]
	v_lshl_add_u64 v[20:21], v[20:21], 0, s[8:9]
	v_lshl_add_u64 v[28:29], v[28:29], 0, s[8:9]
	v_lshl_add_u64 v[26:27], v[26:27], 0, s[8:9]
	v_lshl_add_u64 v[2:3], v[2:3], 0, v[190:191]
	v_lshl_add_u64 v[6:7], v[4:5], 0, v[190:191]
	v_lshl_add_u64 v[10:11], v[10:11], 0, v[190:191]
	v_lshl_add_u64 v[14:15], v[12:13], 0, v[190:191]
	v_lshl_add_u64 v[18:19], v[18:19], 0, v[190:191]
	v_lshl_add_u64 v[22:23], v[20:21], 0, v[190:191]
	v_lshl_add_u64 v[28:29], v[28:29], 0, v[190:191]
	v_lshl_add_u64 v[30:31], v[26:27], 0, v[190:191]
	v_readlane_b32 s30, v255, 57
	s_nop 1
	s_add_i32 s31, s30, 1
	v_writelane_b32 v255, s31, 57
	s_cmp_eq_u32 s30, 1
	s_cbranch_scc0 .Ltkq0_2
	v_mov_b64_e32 v[2:3], v[108:109]
	v_mov_b64_e32 v[4:5], v[110:111]
	s_branch .Ltkq0_e
.Ltkq0_2:
	s_cmp_eq_u32 s30, 2
	s_cbranch_scc0 .Ltkq0_3
	v_mov_b64_e32 v[2:3], v[140:141]
	v_mov_b64_e32 v[4:5], v[142:143]
	s_branch .Ltkq0_e
.Ltkq0_3:
	v_mov_b64_e32 v[2:3], v[214:215]
	v_mov_b64_e32 v[4:5], v[216:217]
.Ltkq0_e:
	s_nop 0
	s_cmp_eq_u32 s30, 1
	s_cbranch_scc0 .Ltkq1_2
	v_mov_b64_e32 v[6:7], v[112:113]
	v_mov_b64_e32 v[8:9], v[114:115]
	s_branch .Ltkq1_e
.Ltkq1_2:
	s_cmp_eq_u32 s30, 2
	s_cbranch_scc0 .Ltkq1_3
	v_mov_b64_e32 v[6:7], v[152:153]
	v_mov_b64_e32 v[8:9], v[154:155]
	s_branch .Ltkq1_e
.Ltkq1_3:
	v_mov_b64_e32 v[6:7], v[218:219]
	v_mov_b64_e32 v[8:9], v[220:221]
; #define GAS __attribute__((address_space(1)))
; #define LAS __attribute__((address_space(3)))
; #define LDS_WAIT() asm volatile("s_waitcnt lgkmcnt(0)" ::: "memory")
; __device__ __forceinline__ void titem_store(const TItem& T, int lane, const f32x4 (&v)[8], LAS float* scr) {
;     const int nblk = T.N / 32, kb = T.item / nblk, nb = T.item % nblk, k0 = 64 * kb, n0 = 32 * nb;
; #pragma unroll
;     for (int i = 0; i < 8; ++i) { LAS float* s = scr + (8 * i + (lane >> 3)) * 33 + 4 * (lane & 7); s[0] = v[i][0]; s[1] = v[i][1]; s[2] = v[i][2]; s[3] = v[i][3]; }
;     LDS_WAIT(); asm volatile("" ::: "memory");
;     const int c = lane & 7;
; #pragma unroll
;     for (int j = 0; j < 4; ++j) { const int n = (lane >> 3) + 8 * j; const LAS float* s = scr + (8 * c) * 33 + n;
;         if (T.f8) { u32x2 o; o.x = pg8::pack4_fp8(s[0 * 33] * pg8::SC_W, s[1 * 33] * pg8::SC_W, s[2 * 33] * pg8::SC_W, s[3 * 33] * pg8::SC_W); o.y = pg8::pack4_fp8(s[4 * 33] * pg8::SC_W, s[5 * 33] * pg8::SC_W, s[6 * 33] * pg8::SC_W, s[7 * 33] * pg8::SC_W);
;             *(GAS u32x2*)((unsigned char*)T.WT + (size_t)row_map(T.mode, n0, n) * 1024 + k0 + 8 * c) = o; }
.Ltkq1_e:
	s_nop 0
	s_cmp_eq_u32 s30, 1
	s_cbranch_scc0 .Ltkq2_2
	v_mov_b64_e32 v[10:11], v[116:117]
	v_mov_b64_e32 v[12:13], v[118:119]
	s_branch .Ltkq2_e
.Ltkq2_2:
	s_cmp_eq_u32 s30, 2
	s_cbranch_scc0 .Ltkq2_3
	v_mov_b64_e32 v[10:11], v[156:157]
	v_mov_b64_e32 v[12:13], v[158:159]
	s_branch .Ltkq2_e
.Ltkq2_3:
	v_mov_b64_e32 v[10:11], v[222:223]
	v_mov_b64_e32 v[12:13], v[224:225]
.Ltkq2_e:
	s_nop 0
	s_cmp_eq_u32 s30, 1
	s_cbranch_scc0 .Ltkq3_2
	v_mov_b64_e32 v[14:15], v[120:121]
	v_mov_b64_e32 v[16:17], v[122:123]
	s_branch .Ltkq3_e
.Ltkq3_2:
	s_cmp_eq_u32 s30, 2
	s_cbranch_scc0 .Ltkq3_3
	v_mov_b64_e32 v[14:15], v[160:161]
	v_mov_b64_e32 v[16:17], v[162:163]
	s_branch .Ltkq3_e
.Ltkq3_3:
	v_mov_b64_e32 v[14:15], v[226:227]
	v_mov_b64_e32 v[16:17], v[228:229]
.Ltkq3_e:
	s_nop 0
	s_cmp_eq_u32 s30, 1
	s_cbranch_scc0 .Ltkq4_2
	v_mov_b64_e32 v[18:19], v[124:125]
	v_mov_b64_e32 v[20:21], v[126:127]
	s_branch .Ltkq4_e
.Ltkq4_2:
	s_cmp_eq_u32 s30, 2
	s_cbranch_scc0 .Ltkq4_3
	v_mov_b64_e32 v[18:19], v[164:165]
	v_mov_b64_e32 v[20:21], v[166:167]
	s_branch .Ltkq4_e
.Ltkq4_3:
	v_mov_b64_e32 v[18:19], v[230:231]
	v_mov_b64_e32 v[20:21], v[232:233]
.Ltkq4_e:
	s_nop 0
	s_cmp_eq_u32 s30, 1
	s_cbranch_scc0 .Ltkq5_2
	v_mov_b64_e32 v[22:23], v[128:129]
	v_mov_b64_e32 v[24:25], v[130:131]
	s_branch .Ltkq5_e
.Ltkq5_2:
	s_cmp_eq_u32 s30, 2
	s_cbranch_scc0 .Ltkq5_3
	v_mov_b64_e32 v[22:23], v[168:169]
	v_mov_b64_e32 v[24:25], v[170:171]
	s_branch .Ltkq5_e
.Ltkq5_3:
	v_mov_b64_e32 v[22:23], v[234:235]
	v_mov_b64_e32 v[24:25], v[236:237]
.Ltkq5_e:
	s_nop 0
	s_cmp_eq_u32 s30, 1
	s_cbranch_scc0 .Ltkq6_2
	v_mov_b64_e32 v[26:27], v[132:133]
	v_mov_b64_e32 v[28:29], v[134:135]
	s_branch .Ltkq6_e
.Ltkq6_2:
	s_cmp_eq_u32 s30, 2
	s_cbranch_scc0 .Ltkq6_3
	v_mov_b64_e32 v[26:27], v[194:195]
	v_mov_b64_e32 v[28:29], v[196:197]
	s_branch .Ltkq6_e
.Ltkq6_3:
	v_mov_b64_e32 v[26:27], v[238:239]
	v_mov_b64_e32 v[28:29], v[240:241]
.Ltkq6_e:
	s_nop 0
	s_cmp_eq_u32 s30, 1
	s_cbranch_scc0 .Ltkq7_2
	v_mov_b64_e32 v[30:31], v[136:137]
	v_mov_b64_e32 v[32:33], v[138:139]
	s_branch .Ltkq7_e
.Ltkq7_2:
	s_cmp_eq_u32 s30, 2
	s_cbranch_scc0 .Ltkq7_3
	v_mov_b64_e32 v[30:31], v[202:203]
	v_mov_b64_e32 v[32:33], v[204:205]
	s_branch .Ltkq7_e
.Ltkq7_3:
	v_mov_b64_e32 v[30:31], v[242:243]
	v_mov_b64_e32 v[32:33], v[244:245]
.Ltkq7_e:
.Ltkser_1528:
	ds_write2_b32 v74, v62, v63 offset1:1
	ds_write2_b32 v74, v64, v65 offset0:2 offset1:3
	v_add_u32_e32 v62, 0x420, v74
	ds_write2_b32 v62, v58, v59 offset1:1
	v_add_u32_e32 v58, 0x428, v74
	ds_write2_b32 v58, v60, v61 offset1:1
	v_add_u32_e32 v58, 0x840, v74
	ds_write2_b32 v58, v54, v55 offset1:1
	v_add_u32_e32 v54, 0x848, v74
	ds_write2_b32 v54, v56, v57 offset1:1
	v_add_u32_e32 v54, 0xc60, v74
	ds_write2_b32 v54, v50, v51 offset1:1
	v_add_u32_e32 v50, 0xc68, v74
	ds_write2_b32 v50, v52, v53 offset1:1
	v_add_u32_e32 v50, 0x1080, v74
	ds_write2_b32 v50, v46, v47 offset1:1
	v_add_u32_e32 v46, 0x1088, v74
	ds_write2_b32 v46, v48, v49 offset1:1
	v_add_u32_e32 v46, 0x14a0, v74
	ds_write2_b32 v46, v42, v43 offset1:1
	v_add_u32_e32 v42, 0x14a8, v74
	ds_write2_b32 v42, v44, v45 offset1:1
	v_add_u32_e32 v42, 0x18c0, v74
	ds_write2_b32 v42, v38, v39 offset1:1
	v_add_u32_e32 v38, 0x18c8, v74
	ds_write2_b32 v38, v40, v41 offset1:1
	v_add_u32_e32 v38, 0x1ce0, v74
	ds_write2_b32 v38, v34, v35 offset1:1
	v_add_u32_e32 v34, 0x1ce8, v74
	ds_write2_b32 v34, v36, v37 offset1:1
	s_waitcnt lgkmcnt(0)
	ds_read2_b32 v[40:41], v69 offset1:33
	ds_read2_b32 v[38:39], v69 offset0:66 offset1:99
	ds_read2_b32 v[36:37], v69 offset0:132 offset1:165
	ds_read2_b32 v[34:35], v69 offset0:198 offset1:231
	s_cmp_lt_i32 s23, 4
	s_cbranch_scc1 .Ltkser_1532
	s_cmp_eq_u32 s23, 4
	s_mov_b64 s[6:7], -1
	s_cbranch_scc0 .Ltkser_1531
	s_mov_b64 s[6:7], 0

; __device__ __forceinline__ void xcd_barrier(const XcdBarrier& b) {
;     asm volatile("s_waitcnt vmcnt(0)" ::: "memory");
;     __syncthreads();
;     if (threadIdx.x == 0) {
;         unsigned* bar = b.bar;
;         __builtin_amdgcn_s_waitcnt(0);
;         unsigned nloc = b.st[0], nx = b.st[1];
;         if (nloc == 0u) { xcd_barrier_complete(bar, b.x, nloc, nx); b.st[0] = nloc; b.st[1] = nx; }
.Ltkser_1560:
	v_mov_b32_e32 v42, v43
	s_branch .Ltkser_1517
.Ltkser_done:
	v_readlane_b32 s0, v255, 13
	s_or_b32 s12, s0, 7
	s_cmp_ge_i32 s12, s93
	s_cbranch_scc1 .LBB0_1388
	s_waitcnt vmcnt(0)
	s_waitcnt vmcnt(0) lgkmcnt(0)
	s_barrier
	s_and_saveexec_b64 s[0:1], s[88:89]
	s_cbranch_execz .LBB0_1387
	v_readlane_b32 s2, v255, 3
	s_waitcnt vmcnt(0) expcnt(0) lgkmcnt(0)
	s_nop 0
	v_mov_b32_e32 v1, s2
	ds_read_b32 v3, v1
	v_readlane_b32 s2, v255, 4
	s_waitcnt lgkmcnt(0)
	v_cmp_ne_u32_e32 vcc, 0, v3
	v_mov_b32_e32 v1, s2
	ds_read_b32 v2, v1
	s_cbranch_vccnz .LBB0_1351
	s_load_dwordx2 s[2:3], s[86:87], 0x4
	s_mov_b32 s9, 1
	s_waitcnt lgkmcnt(0)
	s_mul_i32 s8, s2, s85
	s_mul_i32 s8, s8, s3
	s_branch .LBB0_1339
